# ln3: the 24 row loads per token use the default cache policy instead of nt (y2/s2 were just written; on top of v24)
# baseline (speedup 1.0000x reference)
; __device__ __forceinline__ int otid() { int t = threadIdx.x; asm volatile("" : "+v"(t)); return t; }
; __device__ __forceinline__ void ph_ln3(const Params& p) {
;     const int tid = otid(), wid = tid >> 6, lane = tid & 63;
;     const bf16_t* h = (const bf16_t*)(p.ws + WS_S2); const float* gates = (const float*)(p.ws + WS_GATES); const bf16_t* y2 = (const bf16_t*)p.out; const float* stats2 = (const float*)(p.ws + WS_STATS2);
;     const int rstep = gridDim.x * 8; int row = blockIdx.x * 8 + wid;
;     u32x2 nh[8]; u32x2 na[8], nb[8];
;     if (row < T_TOK) {
; #pragma unroll
;         for (int j = 0; j < 8; ++j) { nh[j] = __builtin_nontemporal_load((const u32x2*)(h + (size_t)row * DM + j * 256 + lane * 4)); na[j] = __builtin_nontemporal_load((const u32x2*)(y2 + (size_t)(2 * row) * DM + j * 256 + lane * 4)); nb[j] = __builtin_nontemporal_load((const u32x2*)(y2 + (size_t)(2 * row + 1) * DM + j * 256 + lane * 4)); } }
.LBB0_1507:
	s_or_b64 exec, exec, s[6:7]
	s_waitcnt lgkmcnt(0)
	s_barrier
	s_mov_b32 s0, 0x8000
	v_ashrrev_i32_e32 v1, 6, v0
	v_lshl_add_u32 v64, s92, 3, v1
	v_cmp_gt_i32_e32 vcc, s0, v64
	s_and_saveexec_b64 s[0:1], vcc
	s_cbranch_execz .LBB0_1514
	s_load_dwordx8 s[4:11], s[70:71], 0xc0
	v_ashrrev_i32_e32 v65, 31, v64
	v_lshlrev_b32_e32 v4, 2, v0
	v_lshlrev_b32_e32 v8, 1, v64
	v_lshlrev_b64 v[2:3], 12, v[64:65]
	v_and_b32_e32 v12, 0xfc, v4
	v_ashrrev_i32_e32 v9, 31, v8
	s_waitcnt lgkmcnt(0)
	v_lshl_add_u64 v[2:3], s[10:11], 0, v[2:3]
	v_lshlrev_b32_e32 v4, 1, v12
	v_mov_b32_e32 v5, 0
	v_lshlrev_b64 v[10:11], 12, v[8:9]
	v_or_b32_e32 v8, 1, v8
	v_lshl_add_u64 v[2:3], v[2:3], 0, v[4:5]
	s_mov_b64 s[16:17], 0x34010000
	v_ashrrev_i32_e32 v9, 31, v8
	s_mov_b32 s0, 0x34010000
	v_lshl_add_u64 v[6:7], v[2:3], 0, s[16:17]
	v_lshlrev_b64 v[8:9], 12, v[8:9]
	v_add_co_u32_e32 v2, vcc, s0, v2
	v_lshl_add_u64 v[10:11], s[8:9], 0, v[10:11]
	v_lshl_add_u64 v[8:9], s[8:9], 0, v[8:9]
	v_addc_co_u32_e32 v3, vcc, 0, v3, vcc
	v_lshl_add_u64 v[10:11], v[10:11], 0, v[4:5]
	v_lshl_add_u64 v[8:9], v[8:9], 0, v[4:5]
	global_load_dwordx2 v[208:209], v[2:3], off
	global_load_dwordx2 v[210:211], v[10:11], off
	global_load_dwordx2 v[204:205], v[10:11], off offset:512
	global_load_dwordx2 v[198:199], v[10:11], off offset:1024
	global_load_dwordx2 v[192:193], v[10:11], off offset:1536
	global_load_dwordx2 v[212:213], v[8:9], off
	global_load_dwordx2 v[206:207], v[8:9], off offset:512
	global_load_dwordx2 v[200:201], v[8:9], off offset:1024
	global_load_dwordx2 v[194:195], v[8:9], off offset:1536
	global_load_dwordx2 v[202:203], v[6:7], off offset:512
	global_load_dwordx2 v[196:197], v[6:7], off offset:1024
	global_load_dwordx2 v[190:191], v[6:7], off offset:1536
	global_load_dwordx2 v[180:181], v[6:7], off offset:2048
	global_load_dwordx2 v[174:175], v[6:7], off offset:2560
	global_load_dwordx2 v[168:169], v[6:7], off offset:3072
	global_load_dwordx2 v[162:163], v[6:7], off offset:3584
	global_load_dwordx2 v[182:183], v[10:11], off offset:2048
	global_load_dwordx2 v[176:177], v[10:11], off offset:2560
	global_load_dwordx2 v[170:171], v[10:11], off offset:3072
	global_load_dwordx2 v[164:165], v[10:11], off offset:3584
	global_load_dwordx2 v[186:187], v[8:9], off offset:2048
	global_load_dwordx2 v[178:179], v[8:9], off offset:2560
	global_load_dwordx2 v[172:173], v[8:9], off offset:3072
	global_load_dwordx2 v[166:167], v[8:9], off offset:3584
	s_load_dwordx4 s[20:23], s[70:71], 0x88
	s_add_u32 s12, s10, 0x44a50000
	s_addc_u32 s13, s11, 0
	s_add_u32 s14, s10, 0x473b0000
	v_lshl_add_u64 v[66:67], s[8:9], 0, v[4:5]
	v_lshlrev_b32_e32 v4, 2, v12
	s_addc_u32 s15, s11, 0
	s_lshl_b32 s0, s94, 3
	s_waitcnt lgkmcnt(0)
	v_lshl_add_u64 v[68:69], s[20:21], 0, v[4:5]
	v_lshl_add_u64 v[70:71], s[22:23], 0, v[4:5]
	v_lshl_add_u64 v[88:89], s[4:5], 0, v[4:5]
	v_lshl_add_u64 v[90:91], s[6:7], 0, v[4:5]
	v_and_b32_e32 v4, 63, v0
	v_lshlrev_b32_e32 v0, 1, v1
	v_lshl_add_u32 v110, s92, 4, v0
	v_add_u32_e32 v0, s0, v64
	v_ashrrev_i32_e32 v1, 31, v0
	v_lshlrev_b64 v[2:3], 13, v[64:65]
	v_lshlrev_b64 v[0:1], 12, v[0:1]
	v_lshl_or_b32 v2, v4, 4, v2
	v_lshl_or_b32 v0, v4, 3, v0
	s_mov_b64 s[2:3], 0x1000
	s_mov_b64 s[18:19], 0x1400
	s_mov_b64 s[20:21], 0x1800
	s_mov_b64 s[22:23], 0x1c00
	v_lshl_add_u64 v[2:3], s[8:9], 0, v[2:3]
	s_ashr_i32 s1, s0, 31
	v_lshl_add_u64 v[0:1], s[10:11], 0, v[0:1]
	v_lshl_add_u64 v[72:73], v[68:69], 0, s[2:3]
	v_lshl_add_u64 v[74:75], v[70:71], 0, s[2:3]
	v_lshl_add_u64 v[76:77], v[68:69], 0, s[18:19]
	v_lshl_add_u64 v[78:79], v[70:71], 0, s[18:19]
	v_lshl_add_u64 v[80:81], v[68:69], 0, s[20:21]
	v_lshl_add_u64 v[82:83], v[70:71], 0, s[20:21]
	v_lshl_add_u64 v[84:85], v[68:69], 0, s[22:23]
	v_lshl_add_u64 v[86:87], v[70:71], 0, s[22:23]
	v_lshl_add_u64 v[92:93], v[88:89], 0, s[2:3]
	v_lshl_add_u64 v[94:95], v[90:91], 0, s[2:3]
	v_lshl_add_u64 v[96:97], v[88:89], 0, s[18:19]
	v_lshl_add_u64 v[98:99], v[90:91], 0, s[18:19]
	v_lshl_add_u64 v[100:101], v[88:89], 0, s[20:21]
	v_lshl_add_u64 v[102:103], v[90:91], 0, s[20:21]
	v_lshl_add_u64 v[104:105], v[88:89], 0, s[22:23]
	v_lshl_add_u64 v[106:107], v[90:91], 0, s[22:23]
	v_lshl_add_u64 v[108:109], v[2:3], 0, s[2:3]
	s_lshl_b64 s[4:5], s[0:1], 13
	s_lshl_b32 s9, s94, 4
	v_lshl_add_u64 v[112:113], v[0:1], 0, s[16:17]
	s_lshl_b64 s[2:3], s[0:1], 12
	s_mov_b64 s[6:7], 0
	s_movk_i32 s1, 0x7fff
	s_mov_b32 s8, 0x3f9837f0
	v_mov_b32_e32 v65, 0x3727c5ac
	s_mov_b32 s16, 0x800000
	s_branch .LBB0_1510

; __device__ __forceinline__ float bflo(unsigned w) { return __uint_as_float(w << 16); }
; __device__ __forceinline__ float bfhi(unsigned w) { return __uint_as_float(w & 0xffff0000u); }
; __device__ __forceinline__ void ph_ln3(const Params& p) {
;     ...
;     for (; row < T_TOK; row += rstep) {
;         const float g0 = gates[row * 2], g1 = gates[row * 2 + 1], m2 = stats2[row * 2], r2 = stats2[row * 2 + 1] * ALPHA; f32x4 v[8];
; #pragma unroll
;         for (int j = 0; j < 8; ++j) { const f32x4 a = (f32x4){bflo(na[j].x), bfhi(na[j].x), bflo(na[j].y), bfhi(na[j].y)}, b = (f32x4){bflo(nb[j].x), bfhi(nb[j].x), bflo(nb[j].y), bfhi(nb[j].y)};
;             const f32x4 gg = *(const f32x4*)(p.ln2_g + j * 256 + lane * 4), bb = *(const f32x4*)(p.ln2_b + j * 256 + lane * 4);
;             v[j] = (((f32x4){bflo(nh[j].x), bfhi(nh[j].x), bflo(nh[j].y), bfhi(nh[j].y)} - m2) * r2) * gg + bb * ALPHA + (a * g0 + b * g1); }
;         if (row + rstep < T_TOK) { const int rn = row + rstep;
; #pragma unroll
;             for (int j = 0; j < 8; ++j) { nh[j] = __builtin_nontemporal_load((const u32x2*)(h + (size_t)rn * DM + j * 256 + lane * 4)); na[j] = __builtin_nontemporal_load((const u32x2*)(y2 + (size_t)(2 * rn) * DM + j * 256 + lane * 4)); nb[j] = __builtin_nontemporal_load((const u32x2*)(y2 + (size_t)(2 * rn + 1) * DM + j * 256 + lane * 4)); } }
.LBB0_1510:
	v_add_u32_e32 v4, 1, v110
	v_ashrrev_i32_e32 v111, 31, v110
	v_ashrrev_i32_e32 v5, 31, v4
	v_lshlrev_b64 v[0:1], 2, v[110:111]
	v_lshlrev_b64 v[4:5], 2, v[4:5]
	v_lshl_add_u64 v[2:3], s[12:13], 0, v[0:1]
	v_lshl_add_u64 v[6:7], s[12:13], 0, v[4:5]
	v_lshl_add_u64 v[0:1], s[14:15], 0, v[0:1]
	v_lshl_add_u64 v[4:5], s[14:15], 0, v[4:5]
	global_load_dword v184, v[2:3], off
	global_load_dword v188, v[6:7], off
	global_load_dword v185, v[0:1], off
	global_load_dword v189, v[4:5], off
	global_load_dwordx4 v[60:63], v[68:69], off
	global_load_dwordx4 v[48:51], v[68:69], off offset:1024
	global_load_dwordx4 v[56:59], v[70:71], off
	global_load_dwordx4 v[52:55], v[70:71], off offset:1024
	global_load_dwordx4 v[40:43], v[68:69], off offset:2048
	global_load_dwordx4 v[32:35], v[68:69], off offset:3072
	global_load_dwordx4 v[44:47], v[70:71], off offset:2048
	global_load_dwordx4 v[36:39], v[70:71], off offset:3072
	global_load_dwordx4 v[24:27], v[72:73], off
	global_load_dwordx4 v[28:31], v[74:75], off
	global_load_dwordx4 v[16:19], v[76:77], off
	global_load_dwordx4 v[20:23], v[78:79], off
	global_load_dwordx4 v[8:11], v[80:81], off
	global_load_dwordx4 v[12:15], v[82:83], off
	global_load_dwordx4 v[0:3], v[84:85], off
	global_load_dwordx4 v[4:7], v[86:87], off
	v_add_u32_e32 v64, s0, v64
	v_cmp_lt_i32_e32 vcc, s1, v64
	s_and_saveexec_b64 s[10:11], vcc
	s_xor_b64 s[10:11], exec, s[10:11]
	v_add_u32_e32 v110, s9, v110
	s_or_saveexec_b64 s[10:11], s[10:11]
	s_and_b64 s[18:19], exec, vcc
	s_or_b64 s[6:7], s[18:19], s[6:7]
	s_waitcnt vmcnt(28)
	v_mov_b64_e32 v[144:145], v[162:163]
	v_mov_b64_e32 v[142:143], v[168:169]
	v_mov_b64_e32 v[140:141], v[174:175]
	v_mov_b64_e32 v[138:139], v[180:181]
	v_mov_b64_e32 v[120:121], v[190:191]
	v_mov_b64_e32 v[118:119], v[196:197]
	v_mov_b64_e32 v[116:117], v[202:203]
	v_mov_b64_e32 v[114:115], v[208:209]
	s_waitcnt vmcnt(24)
	v_mov_b64_e32 v[152:153], v[164:165]
	v_mov_b64_e32 v[150:151], v[170:171]
	v_mov_b64_e32 v[148:149], v[176:177]
	v_mov_b64_e32 v[146:147], v[182:183]
	v_mov_b64_e32 v[128:129], v[192:193]
	v_mov_b64_e32 v[126:127], v[198:199]
	v_mov_b64_e32 v[124:125], v[204:205]
	v_mov_b64_e32 v[122:123], v[210:211]
	s_waitcnt vmcnt(20)
	v_mov_b64_e32 v[160:161], v[166:167]
	v_mov_b64_e32 v[158:159], v[172:173]
	v_mov_b64_e32 v[156:157], v[178:179]
	v_mov_b64_e32 v[154:155], v[186:187]
	v_mov_b64_e32 v[136:137], v[194:195]
	v_mov_b64_e32 v[132:133], v[200:201]
	v_mov_b64_e32 v[130:131], v[206:207]
	v_mov_b64_e32 v[134:135], v[212:213]
	s_xor_b64 exec, exec, s[10:11]
	s_cbranch_execz .LBB0_1509
	v_add_u32_e32 v110, s9, v110
	v_ashrrev_i32_e32 v111, 31, v110
	v_lshlrev_b64 v[114:115], 12, v[110:111]
	v_lshl_add_u64 v[152:153], v[66:67], 0, v[114:115]
	v_add_u32_e32 v114, 1, v110
	v_ashrrev_i32_e32 v115, 31, v114
	v_lshlrev_b64 v[114:115], 12, v[114:115]
	v_lshl_add_u64 v[160:161], v[66:67], 0, v[114:115]
	global_load_dwordx2 v[114:115], v[112:113], off
	global_load_dwordx2 v[116:117], v[112:113], off offset:512
	global_load_dwordx2 v[118:119], v[112:113], off offset:1024
	global_load_dwordx2 v[120:121], v[112:113], off offset:1536
	global_load_dwordx2 v[122:123], v[152:153], off
	global_load_dwordx2 v[124:125], v[152:153], off offset:512
	global_load_dwordx2 v[126:127], v[152:153], off offset:1024
	global_load_dwordx2 v[128:129], v[152:153], off offset:1536
	global_load_dwordx2 v[134:135], v[160:161], off
	global_load_dwordx2 v[130:131], v[160:161], off offset:512
	global_load_dwordx2 v[132:133], v[160:161], off offset:1024
	global_load_dwordx2 v[136:137], v[160:161], off offset:1536
	global_load_dwordx2 v[138:139], v[112:113], off offset:2048
	global_load_dwordx2 v[140:141], v[112:113], off offset:2560
	global_load_dwordx2 v[142:143], v[112:113], off offset:3072
	global_load_dwordx2 v[144:145], v[112:113], off offset:3584
	global_load_dwordx2 v[146:147], v[152:153], off offset:2048
	global_load_dwordx2 v[148:149], v[152:153], off offset:2560
	global_load_dwordx2 v[150:151], v[152:153], off offset:3072
	s_nop 0
	global_load_dwordx2 v[152:153], v[152:153], off offset:3584
	s_nop 0
	global_load_dwordx2 v[154:155], v[160:161], off offset:2048
	global_load_dwordx2 v[156:157], v[160:161], off offset:2560
	global_load_dwordx2 v[158:159], v[160:161], off offset:3072
	s_nop 0
	global_load_dwordx2 v[160:161], v[160:161], off offset:3584
	s_branch .LBB0_1509
